# speedup vs baseline: 1.0139x; 1.0036x over previous
.Lp_fin:
	s_setprio 2
	v_mul_f32_e32 v40, v7, v24
	v_fma_mix_f32 v40, v6, v65, v40 op_sel_hi:[0,1,0]
	v_fma_mix_f32 v40, v5, v64, v40 op_sel:[0,1,0] op_sel_hi:[0,1,0]
	v_fma_mixlo_f16 v40, v4, v64, v40 op_sel_hi:[0,1,0]
	ds_write_b16 v9, v40 offset:0
	v_mul_f32_e32 v41, v7, v25
	v_fma_mix_f32 v41, v6, v69, v41 op_sel_hi:[0,1,0]
	v_fma_mix_f32 v41, v5, v68, v41 op_sel:[0,1,0] op_sel_hi:[0,1,0]
	v_fma_mixlo_f16 v41, v4, v68, v41 op_sel_hi:[0,1,0]
	ds_write_b16 v9, v41 offset:64
	v_mul_f32_e32 v40, v7, v26
	v_fma_mix_f32 v40, v6, v73, v40 op_sel_hi:[0,1,0]
	v_fma_mix_f32 v40, v5, v72, v40 op_sel:[0,1,0] op_sel_hi:[0,1,0]
	v_fma_mixlo_f16 v40, v4, v72, v40 op_sel_hi:[0,1,0]
	ds_write_b16 v9, v40 offset:128
	v_mul_f32_e32 v41, v7, v27
	v_fma_mix_f32 v41, v6, v77, v41 op_sel_hi:[0,1,0]
	v_fma_mix_f32 v41, v5, v76, v41 op_sel:[0,1,0] op_sel_hi:[0,1,0]
	v_fma_mixlo_f16 v41, v4, v76, v41 op_sel_hi:[0,1,0]
	ds_write_b16 v9, v41 offset:192
	v_mul_f32_e32 v40, v7, v28
	v_fma_mix_f32 v40, v6, v81, v40 op_sel_hi:[0,1,0]
	v_fma_mix_f32 v40, v5, v80, v40 op_sel:[0,1,0] op_sel_hi:[0,1,0]
	v_fma_mixlo_f16 v40, v4, v80, v40 op_sel_hi:[0,1,0]
	ds_write_b16 v9, v40 offset:256
	v_mul_f32_e32 v41, v7, v29
	v_fma_mix_f32 v41, v6, v85, v41 op_sel_hi:[0,1,0]
	v_fma_mix_f32 v41, v5, v84, v41 op_sel:[0,1,0] op_sel_hi:[0,1,0]
	v_fma_mixlo_f16 v41, v4, v84, v41 op_sel_hi:[0,1,0]
	ds_write_b16 v9, v41 offset:320
	v_mul_f32_e32 v40, v7, v30
	v_fma_mix_f32 v40, v6, v89, v40 op_sel_hi:[0,1,0]
	v_fma_mix_f32 v40, v5, v88, v40 op_sel:[0,1,0] op_sel_hi:[0,1,0]
	v_fma_mixlo_f16 v40, v4, v88, v40 op_sel_hi:[0,1,0]
	ds_write_b16 v9, v40 offset:384
	v_mul_f32_e32 v41, v7, v31
	v_fma_mix_f32 v41, v6, v93, v41 op_sel_hi:[0,1,0]
	v_fma_mix_f32 v41, v5, v92, v41 op_sel:[0,1,0] op_sel_hi:[0,1,0]
	v_fma_mixlo_f16 v41, v4, v92, v41 op_sel_hi:[0,1,0]
	ds_write_b16 v9, v41 offset:448
	s_branch .Lp_next
